# combine (layer 0): next token's expert ids prefetched before the stores; loop-top wait leaves stores in flight
# baseline (speedup 1.0000x reference)
; template <bool FINAL>
; __device__ __forceinline__ void ph_combine(Frame& F, const bf16* H, bf16* Hout, const float* wn) {
;     int tid_ = threadIdx.x; asm volatile("" : "+v"(tid_)); const int lane_ = tid_ & 63;
;     const bf16* Y = (const bf16*)(KWS + WS_Y); const int* TKE = (const int*)(KWS + WS_TKE); const int* TKS = (const int*)(KWS + WS_TKS); const float* TKG = (const float*)(KWS + WS_TKG); float* RSTD = (float*)(KWS + WS_RSTD);
;     const int gw = blockIdx.x * NWAVES + F.wave, NGW = F.G * NWAVES;
;     f32x4 wv[8];
;     if (FINAL) {
; #pragma unroll
;         for (int j = 0; j < 8; ++j) wv[j] = ((const f32x4*)wn)[lane_ + 64 * j];
;     }
;     for (int t = gw; t < T; t += NGW) {
;         const int r0 = F.MISC[MI_PSTART + TKE[2 * t]] + TKS[2 * t], r1 = F.MISC[MI_PSTART + TKE[2 * t + 1]] + TKS[2 * t + 1]; const float g0 = TKG[2 * t], g1 = TKG[2 * t + 1];
.LBB0_985:
	s_cmp_gt_i32 s30, 11
	s_cselect_b64 s[10:11], -1, 0
	s_cmp_lt_i32 s31, 12
	s_cselect_b64 s[12:13], -1, 0
	s_or_b64 s[10:11], s[10:11], s[12:13]
	s_and_b64 vcc, exec, s[10:11]
	s_cbranch_vccnz .LBB0_1045
	s_lshl_b32 s3, s2, 3
	s_add_i32 s14, s33, s3
	v_mov_b32_e32 v1, v0
	s_cmpk_gt_i32 s14, 0x3fff
	s_cbranch_scc1 .LBB0_991
	s_waitcnt vmcnt(0)
	v_and_b32_e32 v6, 63, v1
	v_mbcnt_lo_u32_b32 v1, -1, 0
	v_mbcnt_hi_u32_b32 v7, -1, v1
	v_and_b32_e32 v1, 64, v7
	v_add_u32_e32 v8, 64, v1
	v_xor_b32_e32 v1, 1, v7
	v_cmp_lt_i32_e32 vcc, v1, v8
	v_xor_b32_e32 v9, 2, v7
	v_xor_b32_e32 v10, 4, v7
	v_cndmask_b32_e32 v1, v7, v1, vcc
	v_cmp_lt_i32_e32 vcc, v9, v8
	s_add_u32 s3, s36, 0x200000
	s_addc_u32 s35, s37, 0
	v_cndmask_b32_e32 v9, v7, v9, vcc
	v_cmp_lt_i32_e32 vcc, v10, v8
	s_add_u32 s40, s36, 0x220000
	s_addc_u32 s41, s37, 0
	v_cndmask_b32_e32 v10, v7, v10, vcc
	v_lshlrev_b32_e32 v58, 2, v10
	v_xor_b32_e32 v10, 8, v7
	v_cmp_lt_i32_e32 vcc, v10, v8
	s_add_u32 s42, s36, 0x240000
	s_addc_u32 s43, s37, 0
	v_cndmask_b32_e32 v10, v7, v10, vcc
	v_lshlrev_b32_e32 v59, 2, v10
	v_xor_b32_e32 v10, 16, v7
	v_cmp_lt_i32_e32 vcc, v10, v8
	s_ashr_i32 s15, s14, 31
	s_lshl_b32 s16, s34, 3
	v_cndmask_b32_e32 v10, v7, v10, vcc
	v_lshlrev_b32_e32 v60, 2, v10
	v_xor_b32_e32 v10, 32, v7
	s_lshl_b64 s[12:13], s[14:15], 2
	v_lshlrev_b32_e32 v2, 3, v6
	v_mov_b32_e32 v3, 0
	v_cmp_lt_i32_e32 vcc, v10, v8
	s_add_u32 s44, s12, 0x260000
	v_lshl_add_u64 v[4:5], s[36:37], 0, v[2:3]
	s_mov_b64 s[10:11], 0x59000000
	v_cndmask_b32_e32 v7, v7, v10, vcc
	s_addc_u32 s45, s13, 0
	s_lshl_b64 s[12:13], s[14:15], 12
	v_lshl_add_u64 v[4:5], v[4:5], 0, s[10:11]
	v_lshlrev_b32_e32 v61, 2, v7
	v_cmp_eq_u32_e64 s[10:11], 0, v6
	s_ashr_i32 s17, s16, 31
	v_or_b32_e32 v6, s12, v2
	v_mov_b32_e32 v7, s13
	s_lshl_b32 s12, s2, 4
	s_lshl_b32 s13, s33, 1
	v_lshlrev_b32_e32 v1, 2, v1
	v_lshlrev_b32_e32 v9, 2, v9
	s_lshl_b64 s[18:19], s[16:17], 2
	s_lshl_b64 s[22:23], s[16:17], 12
	s_add_i32 s24, s12, s13
	s_lshl_b32 s15, s34, 4
	s_add_i32 s17, 0, 0x22000
	s_mov_b32 s46, 0x3c800000
	s_movk_i32 s47, 0x7fff
	s_mov_b32 s48, 0x44800000
	v_mov_b32_e32 v62, 0x358637bd
	s_mov_b32 s49, 0xf800000
	v_mov_b32_e32 v63, 0x260
	v_mov_b32_e32 v64, 1
	s_ashr_i32 s25, s24, 31
	s_lshl_b64 s[12:13], s[24:25], 2
	s_add_u32 s26, s3, s12
	s_addc_u32 s27, s35, s13
	global_load_dwordx2 v[120:121], v3, s[26:27]
	s_waitcnt vmcnt(0)
	s_branch .LBB0_989

; __device__ __forceinline__ float bflo(unsigned w) { return __uint_as_float(w << 16); }
; __device__ __forceinline__ float bfhi(unsigned w) { return __uint_as_float(w & 0xffff0000u); }
; template <bool FINAL>
; __device__ __forceinline__ void ph_combine(Frame& F, const bf16* H, bf16* Hout, const float* wn) {
;     ...
;     for (int t = gw; t < T; t += NGW) {
;         const int r0 = F.MISC[MI_PSTART + TKE[2 * t]] + TKS[2 * t], r1 = F.MISC[MI_PSTART + TKE[2 * t + 1]] + TKS[2 * t + 1]; const float g0 = TKG[2 * t], g1 = TKG[2 * t + 1];
;         const v2u* hr = (const v2u*)(H + (size_t)t * D) + lane_;
;         const v2u* y0 = (const v2u*)(Y + (size_t)r0 * D) + lane_; const v2u* y1 = (const v2u*)(Y + (size_t)r1 * D) + lane_;
;         f32x4 v[8]; float s = 0.f;
; #pragma unroll
;         for (int j = 0; j < 8; ++j) { const v2u a = __builtin_nontemporal_load(y0 + 64 * j), b = __builtin_nontemporal_load(y1 + 64 * j), hh = __builtin_nontemporal_load(hr + 64 * j); f32x4 h = {bflo(hh.x), bfhi(hh.x), bflo(hh.y), bfhi(hh.y)};
;             h.x += g0 * bflo(a.x) + g1 * bflo(b.x); h.y += g0 * bfhi(a.x) + g1 * bfhi(b.x); h.z += g0 * bflo(a.y) + g1 * bflo(b.y); h.w += g0 * bfhi(a.y) + g1 * bfhi(b.y);
.LBB0_989:
	s_ashr_i32 s25, s24, 31
	s_lshl_b64 s[12:13], s[24:25], 2
	s_add_u32 s26, s3, s12
	s_addc_u32 s27, s35, s13
	s_add_u32 s26, s40, s12
	s_addc_u32 s27, s41, s13
	s_add_i32 s50, s24, 1
	s_ashr_i32 s51, s50, 31
	s_lshl_b64 s[50:51], s[50:51], 2
	s_add_u32 s52, s40, s50
	s_addc_u32 s53, s41, s51
	s_add_u32 s12, s42, s12
	s_addc_u32 s13, s43, s13
	s_waitcnt vmcnt(9)
	v_mov_b32_e32 v10, v120
	v_mov_b32_e32 v11, v121
	v_lshlrev_b32_e32 v2, 2, v10
	s_waitcnt lgkmcnt(0)
	v_lshlrev_b32_e32 v8, 2, v11
	v_add_u32_e32 v2, s17, v2
	v_add_u32_e32 v8, s17, v8
	ds_read_b32 v16, v2 offset:64
	global_load_dword v17, v3, s[26:27]
	ds_read_b32 v18, v8 offset:64
	global_load_dword v19, v3, s[52:53]
	v_lshl_add_u64 v[10:11], s[36:37], 0, v[6:7]
	v_add_co_u32_e32 v14, vcc, s46, v10
	s_add_u32 s26, s42, s50
	s_nop 0
	v_addc_co_u32_e32 v15, vcc, 0, v11, vcc
	global_load_dwordx2 v[42:43], v[14:15], off nt
	global_load_dwordx2 v[50:51], v[14:15], off offset:512 nt
	global_load_dwordx2 v[56:57], v[14:15], off offset:1024 nt
	global_load_dwordx2 v[66:67], v[14:15], off offset:1536 nt
	global_load_dwordx2 v[68:69], v[14:15], off offset:2048 nt
	s_addc_u32 s27, s43, s51
	global_load_dword v2, v3, s[12:13]
	global_load_dword v8, v3, s[26:27]
	global_load_dwordx2 v[52:53], v[14:15], off offset:2560 nt
	global_load_dwordx2 v[12:13], v[14:15], off offset:3072 nt
	v_add_co_u32_e32 v10, vcc, s48, v10
	s_waitcnt vmcnt(10) lgkmcnt(1)
	v_add_u32_e32 v16, v17, v16
	v_ashrrev_i32_e32 v17, 31, v16
	s_waitcnt vmcnt(9) lgkmcnt(0)
	v_add_u32_e32 v18, v19, v18
	v_ashrrev_i32_e32 v19, 31, v18
	v_lshlrev_b64 v[16:17], 12, v[16:17]
	v_lshlrev_b64 v[18:19], 12, v[18:19]
	v_lshl_add_u64 v[44:45], v[4:5], 0, v[16:17]
	v_lshl_add_u64 v[48:49], v[4:5], 0, v[18:19]
	global_load_dwordx2 v[36:37], v[44:45], off nt
	global_load_dwordx2 v[38:39], v[48:49], off nt
	global_load_dwordx2 v[34:35], v[44:45], off offset:512 nt
	global_load_dwordx2 v[32:33], v[48:49], off offset:512 nt
	global_load_dwordx2 v[30:31], v[44:45], off offset:1024 nt
	global_load_dwordx2 v[28:29], v[48:49], off offset:1024 nt
	global_load_dwordx2 v[26:27], v[44:45], off offset:1536 nt
	global_load_dwordx2 v[24:25], v[48:49], off offset:1536 nt
	global_load_dwordx2 v[22:23], v[44:45], off offset:2048 nt
	global_load_dwordx2 v[20:21], v[48:49], off offset:2048 nt
	global_load_dwordx2 v[18:19], v[44:45], off offset:2560 nt
	global_load_dwordx2 v[16:17], v[48:49], off offset:2560 nt
	s_waitcnt vmcnt(20)
	v_lshlrev_b32_e32 v41, 16, v43
	global_load_dwordx2 v[14:15], v[14:15], off offset:3584 nt
	s_nop 0
	global_load_dwordx2 v[78:79], v[44:45], off offset:3072 nt
	global_load_dwordx2 v[80:81], v[44:45], off offset:3584 nt
	global_load_dwordx2 v[82:83], v[48:49], off offset:3072 nt
	global_load_dwordx2 v[84:85], v[48:49], off offset:3584 nt
	v_lshlrev_b32_e32 v40, 16, v42
	v_and_b32_e32 v43, 0xffff0000, v43
	v_and_b32_e32 v42, 0xffff0000, v42
	s_waitcnt vmcnt(24)
	v_lshlrev_b32_e32 v47, 16, v51
	v_lshlrev_b32_e32 v46, 16, v50
	v_and_b32_e32 v51, 0xffff0000, v51
	v_and_b32_e32 v50, 0xffff0000, v50
	s_waitcnt vmcnt(23)
	v_lshlrev_b32_e32 v55, 16, v57
	v_lshlrev_b32_e32 v54, 16, v56
	v_and_b32_e32 v57, 0xffff0000, v57
	v_and_b32_e32 v56, 0xffff0000, v56
	s_waitcnt vmcnt(22)
	v_lshlrev_b32_e32 v71, 16, v67
	v_lshlrev_b32_e32 v70, 16, v66
	v_and_b32_e32 v67, 0xffff0000, v67
	v_and_b32_e32 v66, 0xffff0000, v66
	s_waitcnt vmcnt(21)
	v_lshlrev_b32_e32 v73, 16, v69
	v_lshlrev_b32_e32 v72, 16, v68
	v_and_b32_e32 v69, 0xffff0000, v69
	v_and_b32_e32 v68, 0xffff0000, v68
	s_waitcnt vmcnt(18)
	v_lshlrev_b32_e32 v75, 16, v53
	v_lshlrev_b32_e32 v74, 16, v52
	v_and_b32_e32 v53, 0xffff0000, v53
	v_and_b32_e32 v52, 0xffff0000, v52
	v_addc_co_u32_e32 v11, vcc, 0, v11, vcc
	s_waitcnt vmcnt(17)
	v_lshlrev_b32_e32 v77, 16, v13
	v_and_b32_e32 v13, 0xffff0000, v13
	s_waitcnt vmcnt(15)
	v_lshlrev_b32_e32 v49, 16, v39
	v_lshlrev_b32_e32 v48, 16, v38
	v_and_b32_e32 v39, 0xffff0000, v39
	v_and_b32_e32 v38, 0xffff0000, v38
	s_waitcnt vmcnt(13)
	v_lshlrev_b32_e32 v89, 16, v33
	v_lshlrev_b32_e32 v88, 16, v32
	v_and_b32_e32 v33, 0xffff0000, v33
	v_and_b32_e32 v32, 0xffff0000, v32
	v_lshlrev_b32_e32 v87, 16, v35
	v_lshlrev_b32_e32 v45, 16, v37
	v_lshlrev_b32_e32 v44, 16, v36
	v_and_b32_e32 v37, 0xffff0000, v37
	v_and_b32_e32 v36, 0xffff0000, v36
	v_lshlrev_b32_e32 v86, 16, v34
	v_and_b32_e32 v35, 0xffff0000, v35
	v_and_b32_e32 v34, 0xffff0000, v34
	s_waitcnt vmcnt(11)
	v_lshlrev_b32_e32 v93, 16, v29
	v_lshlrev_b32_e32 v92, 16, v28
	v_and_b32_e32 v29, 0xffff0000, v29
	v_and_b32_e32 v28, 0xffff0000, v28
	s_waitcnt vmcnt(9)
	v_lshlrev_b32_e32 v97, 16, v25
	v_lshlrev_b32_e32 v96, 16, v24
	v_and_b32_e32 v25, 0xffff0000, v25
	v_and_b32_e32 v24, 0xffff0000, v24
	s_waitcnt vmcnt(7)
	v_lshlrev_b32_e32 v101, 16, v21
	v_lshlrev_b32_e32 v100, 16, v20
	v_and_b32_e32 v21, 0xffff0000, v21
	v_and_b32_e32 v20, 0xffff0000, v20
	s_waitcnt vmcnt(5)
; __device__ __forceinline__ float bflo(unsigned w) { return __uint_as_float(w << 16); }
; __device__ __forceinline__ float bfhi(unsigned w) { return __uint_as_float(w & 0xffff0000u); }
; template <bool FINAL>
; __device__ __forceinline__ void ph_combine(Frame& F, const bf16* H, bf16* Hout, const float* wn) {
;     ...
;         for (int j = 0; j < 8; ++j) { const v2u a = __builtin_nontemporal_load(y0 + 64 * j), b = __builtin_nontemporal_load(y1 + 64 * j), hh = __builtin_nontemporal_load(hr + 64 * j); f32x4 h = {bflo(hh.x), bfhi(hh.x), bflo(hh.y), bfhi(hh.y)};
;             h.x += g0 * bflo(a.x) + g1 * bflo(b.x); h.y += g0 * bfhi(a.x) + g1 * bfhi(b.x); h.z += g0 * bflo(a.y) + g1 * bflo(b.y); h.w += g0 * bfhi(a.y) + g1 * bfhi(b.y);
;             v[j] = h; s += (h.x * h.x + h.y * h.y) + (h.z * h.z + h.w * h.w); }
	v_lshlrev_b32_e32 v105, 16, v17
	v_lshlrev_b32_e32 v104, 16, v16
	v_and_b32_e32 v17, 0xffff0000, v17
	v_and_b32_e32 v16, 0xffff0000, v16
	v_pk_mul_f32 v[48:49], v[8:9], v[48:49] op_sel_hi:[0,1]
	v_pk_mul_f32 v[38:39], v[8:9], v[38:39] op_sel_hi:[0,1]
	v_pk_mul_f32 v[32:33], v[8:9], v[32:33] op_sel_hi:[0,1]
	v_lshlrev_b32_e32 v91, 16, v31
	v_lshlrev_b32_e32 v90, 16, v30
	v_and_b32_e32 v31, 0xffff0000, v31
	v_and_b32_e32 v30, 0xffff0000, v30
	v_lshlrev_b32_e32 v95, 16, v27
	v_lshlrev_b32_e32 v94, 16, v26
	v_and_b32_e32 v27, 0xffff0000, v27
	v_and_b32_e32 v26, 0xffff0000, v26
	v_lshlrev_b32_e32 v99, 16, v23
	v_lshlrev_b32_e32 v98, 16, v22
	v_and_b32_e32 v23, 0xffff0000, v23
	v_and_b32_e32 v22, 0xffff0000, v22
	v_lshlrev_b32_e32 v103, 16, v19
	v_lshlrev_b32_e32 v102, 16, v18
	v_and_b32_e32 v19, 0xffff0000, v19
	v_and_b32_e32 v18, 0xffff0000, v18
	v_pk_mul_f32 v[88:89], v[8:9], v[88:89] op_sel_hi:[0,1]
	v_pk_mul_f32 v[92:93], v[8:9], v[92:93] op_sel_hi:[0,1]
	v_pk_mul_f32 v[28:29], v[8:9], v[28:29] op_sel_hi:[0,1]
	v_pk_mul_f32 v[96:97], v[8:9], v[96:97] op_sel_hi:[0,1]
	v_pk_mul_f32 v[24:25], v[8:9], v[24:25] op_sel_hi:[0,1]
	v_pk_mul_f32 v[100:101], v[8:9], v[100:101] op_sel_hi:[0,1]
	v_pk_mul_f32 v[20:21], v[8:9], v[20:21] op_sel_hi:[0,1]
	v_pk_mul_f32 v[104:105], v[8:9], v[104:105] op_sel_hi:[0,1]
	v_pk_mul_f32 v[16:17], v[8:9], v[16:17] op_sel_hi:[0,1]
	v_pk_fma_f32 v[44:45], v[2:3], v[44:45], v[48:49] op_sel_hi:[0,1,1]
	v_pk_fma_f32 v[36:37], v[2:3], v[36:37], v[38:39] op_sel_hi:[0,1,1]
	v_pk_fma_f32 v[32:33], v[2:3], v[34:35], v[32:33] op_sel_hi:[0,1,1]
	v_pk_fma_f32 v[38:39], v[2:3], v[86:87], v[88:89] op_sel_hi:[0,1,1]
	v_pk_fma_f32 v[34:35], v[2:3], v[90:91], v[92:93] op_sel_hi:[0,1,1]
	v_pk_fma_f32 v[28:29], v[2:3], v[30:31], v[28:29] op_sel_hi:[0,1,1]
	v_pk_fma_f32 v[30:31], v[2:3], v[94:95], v[96:97] op_sel_hi:[0,1,1]
	v_pk_fma_f32 v[24:25], v[2:3], v[26:27], v[24:25] op_sel_hi:[0,1,1]
	v_pk_fma_f32 v[26:27], v[2:3], v[98:99], v[100:101] op_sel_hi:[0,1,1]
	v_pk_fma_f32 v[20:21], v[2:3], v[22:23], v[20:21] op_sel_hi:[0,1,1]
	v_pk_fma_f32 v[22:23], v[2:3], v[102:103], v[104:105] op_sel_hi:[0,1,1]
	v_pk_fma_f32 v[16:17], v[2:3], v[18:19], v[16:17] op_sel_hi:[0,1,1]
	v_pk_add_f32 v[18:19], v[44:45], v[40:41]
	v_pk_add_f32 v[36:37], v[36:37], v[42:43]
	v_pk_add_f32 v[32:33], v[32:33], v[50:51]
	v_pk_add_f32 v[38:39], v[38:39], v[46:47]
	v_pk_add_f32 v[34:35], v[34:35], v[54:55]
	v_pk_add_f32 v[28:29], v[28:29], v[56:57]
	v_pk_add_f32 v[30:31], v[30:31], v[70:71]
	v_pk_add_f32 v[24:25], v[24:25], v[66:67]
	v_pk_add_f32 v[26:27], v[26:27], v[72:73]
	v_pk_add_f32 v[20:21], v[20:21], v[68:69]
	v_pk_add_f32 v[22:23], v[22:23], v[74:75]
	v_pk_add_f32 v[16:17], v[16:17], v[52:53]
	v_pk_mul_f32 v[40:41], v[36:37], v[36:37]
	v_and_b32_sdwa v52, v19, v64 dst_sel:DWORD dst_unused:UNUSED_PAD src0_sel:WORD_1 src1_sel:DWORD
	v_and_b32_sdwa v53, v18, v64 dst_sel:DWORD dst_unused:UNUSED_PAD src0_sel:WORD_1 src1_sel:DWORD
	v_and_b32_sdwa v54, v37, v64 dst_sel:DWORD dst_unused:UNUSED_PAD src0_sel:WORD_1 src1_sel:DWORD
	v_and_b32_sdwa v55, v36, v64 dst_sel:DWORD dst_unused:UNUSED_PAD src0_sel:WORD_1 src1_sel:DWORD
	v_pk_mul_f32 v[42:43], v[32:33], v[32:33]
	v_and_b32_sdwa v65, v33, v64 dst_sel:DWORD dst_unused:UNUSED_PAD src0_sel:WORD_1 src1_sel:DWORD
	v_and_b32_sdwa v66, v32, v64 dst_sel:DWORD dst_unused:UNUSED_PAD src0_sel:WORD_1 src1_sel:DWORD
	v_and_b32_sdwa v56, v39, v64 dst_sel:DWORD dst_unused:UNUSED_PAD src0_sel:WORD_1 src1_sel:DWORD
	v_and_b32_sdwa v57, v38, v64 dst_sel:DWORD dst_unused:UNUSED_PAD src0_sel:WORD_1 src1_sel:DWORD
	v_pk_mul_f32 v[44:45], v[28:29], v[28:29]
	v_and_b32_sdwa v69, v29, v64 dst_sel:DWORD dst_unused:UNUSED_PAD src0_sel:WORD_1 src1_sel:DWORD
	v_and_b32_sdwa v70, v28, v64 dst_sel:DWORD dst_unused:UNUSED_PAD src0_sel:WORD_1 src1_sel:DWORD
	v_pk_mul_f32 v[46:47], v[24:25], v[24:25]
	v_and_b32_sdwa v71, v31, v64 dst_sel:DWORD dst_unused:UNUSED_PAD src0_sel:WORD_1 src1_sel:DWORD
	v_and_b32_sdwa v72, v30, v64 dst_sel:DWORD dst_unused:UNUSED_PAD src0_sel:WORD_1 src1_sel:DWORD
	v_and_b32_sdwa v73, v25, v64 dst_sel:DWORD dst_unused:UNUSED_PAD src0_sel:WORD_1 src1_sel:DWORD
	v_and_b32_sdwa v74, v24, v64 dst_sel:DWORD dst_unused:UNUSED_PAD src0_sel:WORD_1 src1_sel:DWORD
	v_pk_mul_f32 v[48:49], v[20:21], v[20:21]
	v_and_b32_sdwa v75, v27, v64 dst_sel:DWORD dst_unused:UNUSED_PAD src0_sel:WORD_1 src1_sel:DWORD
	v_and_b32_sdwa v76, v26, v64 dst_sel:DWORD dst_unused:UNUSED_PAD src0_sel:WORD_1 src1_sel:DWORD
	v_and_b32_sdwa v86, v21, v64 dst_sel:DWORD dst_unused:UNUSED_PAD src0_sel:WORD_1 src1_sel:DWORD
	v_and_b32_sdwa v87, v20, v64 dst_sel:DWORD dst_unused:UNUSED_PAD src0_sel:WORD_1 src1_sel:DWORD
	v_pk_mul_f32 v[50:51], v[16:17], v[16:17]
	v_and_b32_sdwa v89, v22, v64 dst_sel:DWORD dst_unused:UNUSED_PAD src0_sel:WORD_1 src1_sel:DWORD
	v_pk_fma_f32 v[40:41], v[18:19], v[18:19], v[40:41]
	v_add3_u32 v53, v18, v53, s47
	v_add3_u32 v52, v19, v52, s47
	v_add3_u32 v37, v37, v54, s47
	v_add3_u32 v36, v36, v55, s47
	v_pk_fma_f32 v[18:19], v[38:39], v[38:39], v[42:43]
	v_add3_u32 v42, v33, v65, s47
	v_add3_u32 v43, v32, v66, s47
	v_and_b32_sdwa v67, v35, v64 dst_sel:DWORD dst_unused:UNUSED_PAD src0_sel:WORD_1 src1_sel:DWORD
	v_and_b32_sdwa v68, v34, v64 dst_sel:DWORD dst_unused:UNUSED_PAD src0_sel:WORD_1 src1_sel:DWORD
	v_and_b32_sdwa v88, v23, v64 dst_sel:DWORD dst_unused:UNUSED_PAD src0_sel:WORD_1 src1_sel:DWORD
	v_add3_u32 v38, v38, v57, s47
	v_add3_u32 v39, v39, v56, s47
	v_pk_fma_f32 v[32:33], v[34:35], v[34:35], v[44:45]
	v_add3_u32 v44, v29, v69, s47
	v_add3_u32 v45, v28, v70, s47
	v_pk_fma_f32 v[28:29], v[30:31], v[30:31], v[46:47]
; __device__ __forceinline__ unsigned pk2(float lo, float hi) { return f2bf(lo) | (f2bf(hi) << 16); }
; template <bool FINAL>
; __device__ __forceinline__ void ph_combine(Frame& F, const bf16* H, bf16* Hout, const float* wn) {
;     ...
;             v[j] = h; s += (h.x * h.x + h.y * h.y) + (h.z * h.z + h.w * h.w); }
;         const float rstd = 1.0f / sqrtf(wave_sum(s) * (1.0f / D) + EPS);
;         if (FINAL) {
;             f32x4* o = (f32x4*)(KOUT + (size_t)t * D) + lane_;
; #pragma unroll
;             for (int j = 0; j < 8; ++j) __builtin_nontemporal_store(v[j] * rstd * wv[j], o + 64 * j);
;         } else {
;             v2u* ho = (v2u*)(Hout + (size_t)t * D) + lane_;
; #pragma unroll
;             for (int j = 0; j < 8; ++j) { v2u o; o.x = pk2(v[j].x, v[j].y); o.y = pk2(v[j].z, v[j].w); ho[64 * j] = o; }
	v_add3_u32 v46, v30, v72, s47
	v_add3_u32 v47, v31, v71, s47
	v_add3_u32 v30, v25, v73, s47
	v_add3_u32 v31, v24, v74, s47
	v_pk_fma_f32 v[24:25], v[26:27], v[26:27], v[48:49]
	v_add3_u32 v48, v26, v76, s47
	v_add3_u32 v49, v27, v75, s47
	v_add3_u32 v26, v21, v86, s47
	v_add3_u32 v27, v20, v87, s47
	v_pk_fma_f32 v[20:21], v[22:23], v[22:23], v[50:51]
	v_add3_u32 v50, v22, v89, s47
	v_and_b32_e32 v22, 0xffff0000, v37
	v_and_b32_e32 v36, 0xffff0000, v36
	v_and_b32_e32 v37, 0xffff0000, v42
	v_and_b32_e32 v42, 0xffff0000, v43
	v_add3_u32 v34, v34, v68, s47
	v_add3_u32 v35, v35, v67, s47
	v_add3_u32 v51, v23, v88, s47
	v_and_b32_e32 v43, 0xffff0000, v44
	v_and_b32_e32 v44, 0xffff0000, v45
	v_and_b32_e32 v45, 0xffff0000, v30
	v_and_b32_e32 v54, 0xffff0000, v31
	v_and_b32_e32 v55, 0xffff0000, v26
	v_and_b32_e32 v56, 0xffff0000, v27
	v_or_b32_sdwa v23, v22, v52 dst_sel:DWORD dst_unused:UNUSED_PAD src0_sel:DWORD src1_sel:WORD_1
	v_or_b32_sdwa v22, v36, v53 dst_sel:DWORD dst_unused:UNUSED_PAD src0_sel:DWORD src1_sel:WORD_1
	v_or_b32_sdwa v27, v37, v39 dst_sel:DWORD dst_unused:UNUSED_PAD src0_sel:DWORD src1_sel:WORD_1
	v_or_b32_sdwa v26, v42, v38 dst_sel:DWORD dst_unused:UNUSED_PAD src0_sel:DWORD src1_sel:WORD_1
	v_or_b32_sdwa v31, v43, v35 dst_sel:DWORD dst_unused:UNUSED_PAD src0_sel:DWORD src1_sel:WORD_1
	v_or_b32_sdwa v30, v44, v34 dst_sel:DWORD dst_unused:UNUSED_PAD src0_sel:DWORD src1_sel:WORD_1
	v_or_b32_sdwa v35, v45, v47 dst_sel:DWORD dst_unused:UNUSED_PAD src0_sel:DWORD src1_sel:WORD_1
	v_or_b32_sdwa v34, v54, v46 dst_sel:DWORD dst_unused:UNUSED_PAD src0_sel:DWORD src1_sel:WORD_1
	v_or_b32_sdwa v37, v55, v49 dst_sel:DWORD dst_unused:UNUSED_PAD src0_sel:DWORD src1_sel:WORD_1
	v_or_b32_sdwa v36, v56, v48 dst_sel:DWORD dst_unused:UNUSED_PAD src0_sel:DWORD src1_sel:WORD_1
	s_add_i32 s98, s24, s15
	s_ashr_i32 s99, s98, 31
	s_lshl_b64 s[98:99], s[98:99], 2
	s_add_u32 s98, s3, s98
	s_addc_u32 s99, s35, s99
	global_load_dwordx2 v[120:121], v3, s[98:99]
	global_store_dwordx2 v[10:11], v[22:23], off
	global_store_dwordx2 v[10:11], v[26:27], off offset:512
	global_store_dwordx2 v[10:11], v[30:31], off offset:1024
	global_store_dwordx2 v[10:11], v[34:35], off offset:1536
	global_store_dwordx2 v[10:11], v[36:37], off offset:2048
	s_waitcnt vmcnt(6)
	v_lshlrev_b32_e32 v27, 16, v83
	v_lshlrev_b32_e32 v26, 16, v82
	v_lshlrev_b32_e32 v23, 16, v79
	v_lshlrev_b32_e32 v22, 16, v78
	v_pk_mul_f32 v[26:27], v[8:9], v[26:27] op_sel_hi:[0,1]
	v_and_b32_e32 v31, 0xffff0000, v83
	v_and_b32_e32 v30, 0xffff0000, v82
	s_waitcnt vmcnt(5)
	v_lshlrev_b32_e32 v37, 16, v85
	v_lshlrev_b32_e32 v36, 16, v84
	v_pk_fma_f32 v[22:23], v[2:3], v[22:23], v[26:27] op_sel_hi:[0,1,1]
	v_and_b32_e32 v27, 0xffff0000, v79
	v_and_b32_e32 v26, 0xffff0000, v78
	v_pk_mul_f32 v[30:31], v[8:9], v[30:31] op_sel_hi:[0,1]
	v_lshlrev_b32_e32 v35, 16, v81
	v_lshlrev_b32_e32 v34, 16, v80
	v_pk_mul_f32 v[36:37], v[8:9], v[36:37] op_sel_hi:[0,1]
	v_pk_fma_f32 v[26:27], v[2:3], v[26:27], v[30:31] op_sel_hi:[0,1,1]
	v_lshlrev_b32_e32 v31, 16, v15
	v_lshlrev_b32_e32 v30, 16, v14
	v_pk_fma_f32 v[34:35], v[2:3], v[34:35], v[36:37] op_sel_hi:[0,1,1]
	v_and_b32_e32 v37, 0xffff0000, v85
	v_and_b32_e32 v36, 0xffff0000, v84
	v_pk_add_f32 v[30:31], v[34:35], v[30:31]
	v_and_b32_e32 v35, 0xffff0000, v81
	v_and_b32_e32 v34, 0xffff0000, v80
	v_pk_mul_f32 v[36:37], v[8:9], v[36:37] op_sel_hi:[0,1]
	v_pk_fma_f32 v[34:35], v[2:3], v[34:35], v[36:37] op_sel_hi:[0,1,1]
	v_add_f32_e32 v2, v18, v19
	v_add_f32_e32 v8, v40, v41
	v_lshlrev_b32_e32 v76, 16, v12
	v_and_b32_e32 v12, 0xffff0000, v12
	v_add_f32_e32 v2, v8, v2
	v_add_f32_e32 v8, v32, v33
	v_pk_add_f32 v[12:13], v[26:27], v[12:13]
	v_and_b32_e32 v15, 0xffff0000, v15
	v_and_b32_e32 v14, 0xffff0000, v14
	v_add_f32_e32 v2, v2, v8
	v_add_f32_e32 v8, v28, v29
	v_pk_add_f32 v[22:23], v[22:23], v[76:77]
	v_pk_mul_f32 v[26:27], v[12:13], v[12:13]
	v_pk_add_f32 v[14:15], v[34:35], v[14:15]
	v_add_f32_e32 v2, v2, v8
	v_add_f32_e32 v8, v24, v25
	v_pk_fma_f32 v[26:27], v[22:23], v[22:23], v[26:27]
	v_pk_mul_f32 v[34:35], v[14:15], v[14:15]
	v_add_f32_e32 v2, v2, v8
	v_add_f32_e32 v8, v20, v21
	v_pk_fma_f32 v[34:35], v[30:31], v[30:31], v[34:35]
	v_add_f32_e32 v2, v2, v8
	v_add_f32_e32 v8, v26, v27
	v_add_f32_e32 v2, v2, v8
	v_add_f32_e32 v8, v34, v35
	v_add_f32_e32 v2, v2, v8
	ds_bpermute_b32 v8, v1, v2
	v_and_b32_sdwa v90, v17, v64 dst_sel:DWORD dst_unused:UNUSED_PAD src0_sel:WORD_1 src1_sel:DWORD
	v_and_b32_sdwa v91, v16, v64 dst_sel:DWORD dst_unused:UNUSED_PAD src0_sel:WORD_1 src1_sel:DWORD
	v_add3_u32 v17, v17, v90, s47
	v_add3_u32 v16, v16, v91, s47
	s_waitcnt lgkmcnt(0)
	v_add_f32_e32 v2, v2, v8
	ds_bpermute_b32 v8, v9, v2
	v_and_b32_e32 v17, 0xffff0000, v17
	v_and_b32_e32 v16, 0xffff0000, v16
	v_or_b32_sdwa v17, v17, v51 dst_sel:DWORD dst_unused:UNUSED_PAD src0_sel:DWORD src1_sel:WORD_1
	v_or_b32_sdwa v16, v16, v50 dst_sel:DWORD dst_unused:UNUSED_PAD src0_sel:DWORD src1_sel:WORD_1
	s_waitcnt lgkmcnt(0)
	v_add_f32_e32 v2, v2, v8
	ds_bpermute_b32 v8, v58, v2
	v_and_b32_sdwa v18, v13, v64 dst_sel:DWORD dst_unused:UNUSED_PAD src0_sel:WORD_1 src1_sel:DWORD
	v_and_b32_sdwa v19, v12, v64 dst_sel:DWORD dst_unused:UNUSED_PAD src0_sel:WORD_1 src1_sel:DWORD
	global_store_dwordx2 v[10:11], v[16:17], off offset:2560
	v_and_b32_sdwa v16, v23, v64 dst_sel:DWORD dst_unused:UNUSED_PAD src0_sel:WORD_1 src1_sel:DWORD
	s_waitcnt lgkmcnt(0)
	v_add_f32_e32 v2, v2, v8
	ds_bpermute_b32 v8, v59, v2
	v_and_b32_sdwa v17, v22, v64 dst_sel:DWORD dst_unused:UNUSED_PAD src0_sel:WORD_1 src1_sel:DWORD
	v_add3_u32 v13, v13, v18, s47
	v_add3_u32 v12, v12, v19, s47
	v_add3_u32 v17, v22, v17, s47
	s_waitcnt lgkmcnt(0)
	v_add_f32_e32 v2, v2, v8
	ds_bpermute_b32 v8, v60, v2
	v_add3_u32 v16, v23, v16, s47
	v_and_b32_e32 v13, 0xffff0000, v13
	v_and_b32_e32 v12, 0xffff0000, v12
	v_or_b32_sdwa v13, v13, v16 dst_sel:DWORD dst_unused:UNUSED_PAD src0_sel:DWORD src1_sel:WORD_1
	v_or_b32_sdwa v12, v12, v17 dst_sel:DWORD dst_unused:UNUSED_PAD src0_sel:DWORD src1_sel:WORD_1
	s_waitcnt lgkmcnt(0)
	v_add_f32_e32 v2, v2, v8
	global_store_dwordx2 v[10:11], v[12:13], off offset:3072
	ds_bpermute_b32 v8, v61, v2
	v_and_b32_sdwa v13, v30, v64 dst_sel:DWORD dst_unused:UNUSED_PAD src0_sel:WORD_1 src1_sel:DWORD
	v_add3_u32 v16, v30, v13, s47
	v_and_b32_sdwa v13, v15, v64 dst_sel:DWORD dst_unused:UNUSED_PAD src0_sel:WORD_1 src1_sel:DWORD
	v_and_b32_sdwa v17, v14, v64 dst_sel:DWORD dst_unused:UNUSED_PAD src0_sel:WORD_1 src1_sel:DWORD
	v_and_b32_sdwa v12, v31, v64 dst_sel:DWORD dst_unused:UNUSED_PAD src0_sel:WORD_1 src1_sel:DWORD
	v_add3_u32 v13, v15, v13, s47
	v_add3_u32 v14, v14, v17, s47
	v_add3_u32 v12, v31, v12, s47
	v_and_b32_e32 v13, 0xffff0000, v13
	v_and_b32_e32 v14, 0xffff0000, v14
	v_or_b32_sdwa v13, v13, v12 dst_sel:DWORD dst_unused:UNUSED_PAD src0_sel:DWORD src1_sel:WORD_1
	v_or_b32_sdwa v12, v14, v16 dst_sel:DWORD dst_unused:UNUSED_PAD src0_sel:DWORD src1_sel:WORD_1
	global_store_dwordx2 v[10:11], v[12:13], off offset:3584
	s_and_saveexec_b64 s[26:27], s[10:11]
	s_cbranch_execz .LBB0_988
; __device__ __forceinline__ unsigned pk2(float lo, float hi) { return f2bf(lo) | (f2bf(hi) << 16); }
; template <bool FINAL>
; __device__ __forceinline__ void ph_combine(Frame& F, const bf16* H, bf16* Hout, const float* wn) {
;     ...
;         const float rstd = 1.0f / sqrtf(wave_sum(s) * (1.0f / D) + EPS);
;         if (FINAL) {
;             f32x4* o = (f32x4*)(KOUT + (size_t)t * D) + lane_;
; #pragma unroll
;             for (int j = 0; j < 8; ++j) __builtin_nontemporal_store(v[j] * rstd * wv[j], o + 64 * j);
;         } else {
;             v2u* ho = (v2u*)(Hout + (size_t)t * D) + lane_;
; #pragma unroll
;             for (int j = 0; j < 8; ++j) { v2u o; o.x = pk2(v[j].x, v[j].y); o.y = pk2(v[j].z, v[j].w); ho[64 * j] = o; }
;             if (lane_ == 0) RSTD[t] = rstd;
	s_waitcnt lgkmcnt(0)
	v_add_f32_e32 v2, v2, v8
	v_fmamk_f32 v2, v2, 0x3a000000, v62
	v_mul_f32_e32 v8, 0x4f800000, v2
	v_cmp_gt_f32_e32 vcc, s49, v2
	s_nop 1
	v_cndmask_b32_e32 v2, v2, v8, vcc
	v_sqrt_f32_e32 v8, v2
	s_nop 0
	v_add_u32_e32 v10, -1, v8
	v_fma_f32 v12, -v10, v8, v2
	v_add_u32_e32 v11, 1, v8
	v_cmp_ge_f32_e64 s[12:13], 0, v12
	s_nop 1
	v_cndmask_b32_e64 v10, v8, v10, s[12:13]
	v_fma_f32 v8, -v11, v8, v2
	v_cmp_lt_f32_e64 s[12:13], 0, v8
	s_nop 1
	v_cndmask_b32_e64 v8, v10, v11, s[12:13]
	v_mul_f32_e32 v10, 0x37800000, v8
	v_cndmask_b32_e32 v8, v8, v10, vcc
	v_cmp_class_f32_e32 vcc, v2, v63
	s_nop 1
	v_cndmask_b32_e32 v2, v8, v2, vcc
	v_div_scale_f32 v8, s[12:13], v2, v2, 1.0
	v_rcp_f32_e32 v10, v8
	s_add_u32 s12, s36, s44
	s_addc_u32 s13, s37, s45
	v_fma_f32 v11, -v8, v10, 1.0
	v_fmac_f32_e32 v10, v11, v10
	v_div_scale_f32 v11, vcc, 1.0, v2, 1.0
	v_mul_f32_e32 v12, v11, v10
	v_fma_f32 v13, -v8, v12, v11
	v_fmac_f32_e32 v12, v13, v10
	v_fma_f32 v8, -v8, v12, v11
	v_div_fmas_f32 v8, v8, v10, v12
	v_div_fixup_f32 v2, v8, v2, 1.0
	global_store_dword v3, v2, s[12:13]
	s_branch .LBB0_988
